# static s_setprio 1 for waves 4-7 (younger half) across the P4 mLSTM phase, reset at phase end
# speedup vs baseline: 1.0022x; 1.0022x over previous
.LBB0_609:
	s_or_b64 exec, exec, s[0:1]
	v_mov_b32_e32 v108, v0
	s_waitcnt lgkmcnt(0)
	v_mov_b32_e32 v1, s76
	v_mov_b32_e32 v2, s77
	s_barrier
	s_add_i32 s0, 0, 0x25d38
	v_readfirstlane_b32 s1, v2
	v_mov_b32_e32 v2, s78
	v_mov_b32_e32 v4, s74
	v_mov_b32_e32 v5, s75
	v_mov_b32_e32 v2, s0
	ds_read_b64 v[2:3], v2
	v_readfirstlane_b32 s46, v4
	v_readfirstlane_b32 s2, v1
	v_readfirstlane_b32 s39, v5
	s_mov_b32 s35, 0
	s_waitcnt lgkmcnt(0)
	v_readfirstlane_b32 s4, v2
	v_readfirstlane_b32 s5, v3
	s_cmpk_gt_i32 s46, 0xff
	v_writelane_b32 v243, s4, 14
	v_readfirstlane_b32 s3, v108
	s_nop 0
	v_writelane_b32 v243, s5, 15
	s_cbranch_scc1 .LBB0_825
	v_readfirstlane_b32 s98, v0
	s_nop 3
	s_cmp_lt_u32 s98, 0x100
	s_cbranch_scc1 .Lp4prio0
	s_setprio 1
.Lp4prio0:
	s_add_u32 s4, s2, 0x7400000
	s_addc_u32 s5, s1, 0
	s_add_u32 s40, s2, 0x17e00000
	s_addc_u32 s41, s1, 0
	s_add_u32 s0, s2, 0x300000
	v_writelane_b32 v243, s0, 16
	s_addc_u32 s0, s1, 0
	v_writelane_b32 v243, s0, 17
	s_add_u32 s0, s2, 0x1a200000
	v_writelane_b32 v243, s0, 19
	s_addc_u32 s0, s1, 0
	s_ashr_i32 s28, s3, 6
	v_writelane_b32 v243, s0, 20
	s_mul_i32 s0, s28, 0x2080
	s_add_i32 s0, s0, 0
	s_add_i32 s47, s0, 0x14f00
	s_lshl_b32 s0, s46, 3
	s_add_i32 s42, s28, s0
	s_lshl_b32 s33, s39, 3
	s_cmpk_eq_i32 s39, 0x100
	s_cselect_b64 s[8:9], -1, 0
	s_and_b64 s[6:7], s[8:9], exec
	s_movk_i32 s0, 0x330
	v_cmp_gt_i32_e64 s[6:7], s0, v108
	v_and_b32_e32 v1, 3, v108
	s_cselect_b32 s16, 0x4800, 0
	v_writelane_b32 v243, s6, 21
	s_cselect_b32 s18, 0xffffb800, 0
	s_lshl_b32 s17, s28, 4
	v_writelane_b32 v243, s7, 22
	v_cmp_eq_u32_e64 s[6:7], 0, v1
	v_ashrrev_i32_e32 v123, 2, v108
	s_movk_i32 s0, 0x70
	v_writelane_b32 v243, s6, 23
	s_cmp_gt_u32 s3, 63
	v_and_b32_e32 v111, 63, v108
	v_writelane_b32 v243, s7, 24
	s_movk_i32 s6, 0x8ff
	v_cmp_lt_i32_e64 s[6:7], s6, v108
	v_mul_lo_u32 v2, v123, s0
	v_add_u32_e32 v110, 0, v2
	v_writelane_b32 v243, s6, 25
	v_lshlrev_b32_e32 v2, 1, v111
	v_lshlrev_b32_e32 v112, 3, v1
	v_writelane_b32 v243, s7, 26
	s_cselect_b64 s[6:7], -1, 0
	s_cmp_lt_u32 s3, 64
	s_cselect_b64 s[10:11], -1, 0
	s_add_i32 s29, 0, 0x10700
	s_movk_i32 s3, 0xa0
	v_sub_u32_e32 v156, 0, v2
	v_mad_u64_u32 v[2:3], s[14:15], v123, s3, v[110:111]
	v_lshlrev_b32_e32 v118, 4, v1
	s_add_u32 s43, s2, 0x2ce00000
	v_and_b32_e32 v1, 7, v108
	v_bfe_u32 v158, v108, 3, 3
	s_addc_u32 s44, s1, 0
	v_mul_u32_u24_e32 v3, 0x410, v1
	v_lshlrev_b32_e32 v7, 2, v158
	s_add_i32 s1, 0, 0x8800
	v_add3_u32 v159, s47, v3, v7
	v_add_u32_e32 v3, s1, v112
	s_lshl_b32 s2, s28, 5
	s_mul_i32 s1, s39, 0x88
	s_add_i32 s2, s2, 0
	s_add_i32 s19, s42, s1
	v_bfe_u32 v113, v108, 4, 2
	s_cmp_lt_i32 s19, s16
	v_and_b32_e32 v117, 15, v108
	v_lshlrev_b32_e32 v122, 2, v113
	s_cselect_b64 s[14:15], -1, 0
	v_or_b32_e32 v151, s17, v117
	v_or_b32_e32 v7, s17, v122
	s_and_b64 s[16:17], s[14:15], exec
	s_cselect_b32 s1, 0, s18
	s_add_i32 s3, s1, s19
	s_mul_hi_i32 s1, s3, 0x30c30c31
	s_and_b64 s[20:21], s[8:9], s[14:15]
	s_lshr_b32 s14, s1, 31
	s_ashr_i32 s1, s1, 10
	s_add_i32 s1, s1, s14
	v_writelane_b32 v243, s10, 27
	s_mul_i32 s14, s1, 0xffffeb00
	s_add_i32 s31, s14, s3
	v_writelane_b32 v243, s11, 28
	s_and_b64 s[14:15], s[20:21], exec
	v_writelane_b32 v243, s20, 29
	v_cmp_gt_i32_e64 s[50:51], v122, v151
	v_lshl_add_u32 v11, v7, 1, 0
	v_writelane_b32 v243, s21, 30
	v_writelane_b32 v243, s50, 31
	v_or_b32_e32 v7, 2, v122
	s_brev_b32 s3, 16
	v_writelane_b32 v243, s51, 32
	v_cmp_lt_i32_e64 s[50:51], v122, v151
	s_cselect_b32 s3, s3, 0xc600000
	s_lshl_b32 s14, s31, 1
	v_writelane_b32 v243, s50, 33
	s_add_i32 s14, s14, 0x7fffe400
	s_and_b32 s30, s14, 0x7fffffc0
	v_writelane_b32 v243, s51, 34
	v_cmp_gt_i32_e64 s[50:51], v7, v151
	v_or_b32_e32 v7, 3, v122
	s_lshl_b32 s14, s19, 5
	v_writelane_b32 v243, s50, 35
	s_and_b32 s34, s14, 0x3e0
	s_and_b64 s[14:15], s[20:21], exec
	v_writelane_b32 v243, s51, 36
	v_cmp_gt_i32_e64 s[50:51], v7, v151
	v_or_b32_e32 v7, 16, v122
	s_mov_b32 s16, 0x1000000
	v_writelane_b32 v243, s50, 37
	s_mul_hi_i32 s14, s31, 0x92492493
	s_cselect_b32 s36, s16, 0xb800000
	v_writelane_b32 v243, s51, 38
	v_cmp_gt_i32_e64 s[50:51], v7, v151
	v_or_b32_e32 v7, 17, v122
	s_add_i32 s14, s14, s31
	v_writelane_b32 v243, s50, 39
	s_lshr_b32 s15, s14, 31
	s_ashr_i32 s14, s14, 7
	v_writelane_b32 v243, s51, 40
	v_cmp_gt_i32_e64 s[50:51], v7, v151
	v_or_b32_e32 v7, 18, v122
	s_add_i32 s14, s14, s15
	v_writelane_b32 v243, s50, 41
	s_lshl_b32 s37, s14, 6
	s_mulk_i32 s14, 0xe0
	v_writelane_b32 v243, s51, 42
	v_cmp_gt_i32_e64 s[50:51], v7, v151
	v_or_b32_e32 v7, 19, v122
	s_sub_i32 s14, s31, s14
	v_writelane_b32 v243, s50, 43
	s_lshl_b32 s38, s14, 5
	s_cmp_gt_i32 s28, -1
	v_writelane_b32 v243, s51, 44
	v_cmp_gt_i32_e64 s[50:51], v7, v151
	v_or_b32_e32 v7, 32, v122
	s_cselect_b64 s[84:85], -1, 0
	v_writelane_b32 v243, s50, 45
	s_cmp_gt_i32 s28, 0
	s_cselect_b64 s[14:15], -1, 0
	v_writelane_b32 v243, s51, 46
	v_cmp_gt_i32_e64 s[50:51], v7, v151
	v_or_b32_e32 v7, 33, v122
	s_cmp_gt_i32 s28, 1
	v_writelane_b32 v243, s50, 47
	s_cselect_b64 s[16:17], -1, 0
	s_cmp_gt_i32 s28, 2
	v_writelane_b32 v243, s51, 48
	v_cmp_gt_i32_e64 s[50:51], v7, v151
	v_or_b32_e32 v7, 34, v122
	s_cselect_b64 s[18:19], -1, 0
	v_writelane_b32 v243, s50, 49
	s_cmp_gt_i32 s28, 3
	s_cselect_b64 s[20:21], -1, 0
	v_writelane_b32 v243, s51, 50
	v_cmp_gt_i32_e64 s[50:51], v7, v151
	v_or_b32_e32 v7, 35, v122
	s_cmp_gt_i32 s28, 4
	v_writelane_b32 v243, s50, 51
	s_cselect_b64 s[22:23], -1, 0
	s_cmp_gt_i32 s28, 5
	v_writelane_b32 v243, s51, 52
	v_cmp_gt_i32_e64 s[50:51], v7, v151
	v_or_b32_e32 v7, 48, v122
	v_bfe_u32 v5, v108, 2, 2
	v_writelane_b32 v243, s50, 53
	v_lshlrev_b32_e32 v116, 3, v113
	v_lshlrev_b32_e32 v6, 2, v111
	v_writelane_b32 v243, s51, 54
	v_cmp_gt_i32_e64 s[50:51], v7, v151
	v_or_b32_e32 v7, 49, v122
	s_cselect_b64 s[24:25], -1, 0
	v_writelane_b32 v243, s50, 55
	s_cmp_gt_i32 s28, 6
	v_add_u32_e32 v153, s29, v6
	v_writelane_b32 v243, s51, 56
	v_cmp_gt_i32_e64 s[50:51], v7, v151
	v_or_b32_e32 v7, 50, v122
	v_add_u32_e32 v155, 0, v6
	v_writelane_b32 v243, s50, 57
	v_and_b32_e32 v163, 28, v6
	v_or_b32_e32 v6, v116, v5
	v_writelane_b32 v243, s51, 58
	v_cmp_gt_i32_e64 s[50:51], v7, v151
	v_or_b32_e32 v7, 51, v122
	s_cselect_b64 s[26:27], -1, 0
	v_writelane_b32 v243, s50, 59
	s_cmpk_lt_i32 s31, 0xe00
	v_or_b32_e32 v5, v122, v5
	v_writelane_b32 v243, s51, 60
	v_cmp_gt_i32_e64 s[50:51], v7, v151
	v_or_b32_e32 v7, 64, v122
	v_mad_u32_u24 v164, v5, s0, v3
	v_writelane_b32 v243, s50, 61
	v_mul_u32_u24_e32 v5, 0x110, v6
	v_mad_u32_u24 v169, v6, s0, v3
	v_writelane_b32 v243, s51, 62
	v_cmp_gt_i32_e64 s[50:51], v7, v151
	v_or_b32_e32 v7, 0x41, v122
	s_movk_i32 s0, 0x400
	v_writelane_b32 v243, s50, 63
	s_cselect_b32 s3, s36, s3
	s_mov_b32 s31, 0xe00000
	v_writelane_b32 v242, s51, 0
	v_cmp_gt_i32_e64 s[50:51], v7, v151
	v_or_b32_e32 v7, 0x42, v122
	v_add3_u32 v168, s2, v112, v5
	v_writelane_b32 v242, s50, 1
	s_cselect_b32 s2, s0, 0xe00
	s_cselect_b32 s0, s37, s30
	v_writelane_b32 v242, s51, 2
	v_cmp_gt_i32_e64 s[50:51], v7, v151
	v_or_b32_e32 v7, 0x43, v122
	s_cselect_b32 s30, s38, s34
	v_writelane_b32 v242, s50, 3
	s_cselect_b32 s31, s31, 0x700000
	s_add_u32 s3, s43, s3
	v_writelane_b32 v242, s51, 4
	v_cmp_gt_i32_e64 s[50:51], v7, v151
	v_or_b32_e32 v7, 0x50, v122
	v_cmp_gt_i32_e64 s[56:57], v7, v151
	v_or_b32_e32 v7, 0x51, v122
	v_cmp_gt_i32_e64 s[58:59], v7, v151
	v_or_b32_e32 v7, 0x52, v122
	v_cmp_gt_i32_e64 s[60:61], v7, v151
	v_or_b32_e32 v7, 0x53, v122
	v_cmp_gt_i32_e64 s[62:63], v7, v151
	v_or_b32_e32 v7, 0x60, v122
	v_cmp_gt_i32_e64 s[64:65], v7, v151
	v_or_b32_e32 v7, 0x61, v122
	v_cmp_gt_i32_e64 s[66:67], v7, v151
	v_or_b32_e32 v7, 0x62, v122
	s_addc_u32 s34, s44, 0
	s_mul_hi_i32 s36, s31, s1
	s_mul_i32 s31, s31, s1
	v_cmp_gt_i32_e64 s[68:69], v7, v151
	v_or_b32_e32 v7, 0x63, v122
	s_add_u32 s3, s3, s31
	v_cmp_gt_i32_e64 s[70:71], v7, v151
	v_or_b32_e32 v7, 0x70, v122
	s_addc_u32 s31, s34, s36
	s_ashr_i32 s1, s0, 31
	v_cmp_gt_i32_e64 s[72:73], v7, v151
	v_or_b32_e32 v7, 0x71, v122
	s_lshl_b64 s[0:1], s[0:1], 1
	v_mov_b32_e32 v115, 0
	v_and_b32_e32 v114, 48, v108
	v_cmp_gt_i32_e64 s[74:75], v7, v151
	v_or_b32_e32 v7, 0x72, v122
	s_add_u32 s0, s3, s0
	v_lshlrev_b32_e32 v4, 3, v1
	v_or_b32_e32 v160, 8, v158
	v_lshl_add_u64 v[120:121], s[40:41], 0, v[114:115]
	v_add_u32_e32 v10, 0, v114
	v_cmp_gt_i32_e64 s[76:77], v7, v151
	v_or_b32_e32 v7, 0x73, v122
	s_addc_u32 s1, s31, s1
	v_lshlrev_b32_e32 v114, 4, v1
	v_or_b32_e32 v1, s30, v158
	v_or_b32_e32 v161, 16, v158
	v_cmp_gt_i32_e64 s[78:79], v7, v151
	v_lshl_add_u64 v[6:7], s[0:1], 0, v[114:115]
	v_mad_i64_i32 v[8:9], s[0:1], s2, v1, 0
	v_or_b32_e32 v1, s30, v160
	v_or_b32_e32 v162, 24, v158
	v_lshl_add_u64 v[124:125], v[8:9], 1, v[6:7]
	v_mad_i64_i32 v[8:9], s[0:1], s2, v1, 0
	v_or_b32_e32 v1, s30, v161
	v_writelane_b32 v242, s50, 5
	v_lshl_add_u64 v[126:127], v[8:9], 1, v[6:7]
	v_mad_i64_i32 v[8:9], s[0:1], s2, v1, 0
	v_or_b32_e32 v1, s30, v162
	v_writelane_b32 v242, s51, 6
	v_lshl_add_u64 v[128:129], v[8:9], 1, v[6:7]
	v_mad_i64_i32 v[8:9], s[0:1], s2, v1, 0
	v_max_i32_e32 v1, 0x700, v108
	v_writelane_b32 v242, s43, 7
	v_sub_u32_e32 v1, v1, v108
	v_writelane_b32 v242, s44, 9
	s_lshl_b32 s0, s42, 5
	v_add_u32_e32 v1, 0x1ff, v1
	v_lshlrev_b32_e32 v176, 2, v108
	v_lshl_add_u64 v[130:131], v[8:9], 1, v[6:7]
	v_writelane_b32 v242, s42, 10
	s_and_b32 s0, s0, 0x3e0
	v_add_u32_e32 v3, 0, v176
	v_lshlrev_b32_e32 v8, 2, v1
	v_writelane_b32 v242, s0, 11
	v_add_u32_e32 v3, 0x12b00, v3
	s_movk_i32 s0, 0xdff
	v_and_b32_e32 v8, 0xfffff800, v8
	v_lshrrev_b32_e32 v5, 9, v1
	v_cmp_lt_u32_e32 vcc, s0, v1
	v_cmp_gt_u32_e64 s[0:1], 2.0, v1
	v_add_u32_e32 v1, v3, v8
	v_add_u32_e32 v6, 1, v5
	v_add_u32_e32 v5, -1, v5
	v_cmp_ge_u32_e64 s[2:3], v1, v3
	s_and_b64 s[0:1], s[2:3], s[0:1]
	v_cmp_lt_u32_e64 s[2:3], 1, v5
	v_lshrrev_b32_e32 v7, 1, v5
	v_and_b32_e32 v5, 2, v5
	v_writelane_b32 v242, s2, 13
	v_and_b32_e32 v3, 0xfffffe, v6
	s_and_b64 s[0:1], vcc, s[0:1]
	v_writelane_b32 v242, s3, 14
	v_cmp_eq_u32_e64 s[2:3], 0, v5
	v_mov_b32_e32 v119, v115
	v_and_b32_e32 v12, 0x7f, v108
	v_writelane_b32 v242, s2, 15
	v_lshl_add_u32 v177, v3, 9, v108
	v_mul_u32_u24_e32 v13, 0x110, v117
	v_writelane_b32 v242, s3, 16
	v_cmp_ne_u32_e64 s[2:3], v6, v3
	v_lshl_add_u32 v3, v108, 4, 0
	v_or_b32_e32 v132, 0xffffff00, v12
	v_writelane_b32 v242, s2, 17
	v_add_u32_e32 v7, 1, v7
	v_add_u32_e32 v179, 0xc000, v3
	v_writelane_b32 v242, s3, 18
	v_writelane_b32 v242, s0, 19
	v_mbcnt_hi_u32_b32 v184, -1, v212
	v_bfrev_b32_e32 v6, 0.5
	v_writelane_b32 v242, s1, 20
	v_writelane_b32 v242, s40, 21
	s_lshl_b32 s1, s28, 1
	s_movk_i32 s49, 0x100
	v_writelane_b32 v242, s41, 22
	v_lshl_add_u64 v[134:135], s[40:41], 0, v[118:119]
	s_lshl_b32 s41, s39, 4
	v_writelane_b32 v242, s39, 23
	s_sub_i32 s0, 0, s41
	v_writelane_b32 v242, s0, 24
	s_lshl_b32 s0, s46, 4
	s_add_i32 s0, s0, s1
	s_add_i32 s0, s0, 0x7fffe400
	v_writelane_b32 v242, s0, 25
	s_add_i32 s0, 0, 0x25de0
	v_writelane_b32 v242, s0, 27
	s_add_i32 s0, 0, 0x25dd0
	v_writelane_b32 v242, s0, 29
	s_add_i32 s0, s47, 0x820
	v_writelane_b32 v242, s0, 30
	s_add_i32 s0, s47, 0xc30
	v_writelane_b32 v242, s0, 31
	s_add_i32 s0, s47, 0x1040
	v_writelane_b32 v242, s0, 33
	s_add_i32 s0, s47, 0x1450
	v_writelane_b32 v242, s0, 34
	s_add_i32 s0, s47, 0x1860
	v_writelane_b32 v242, s0, 35
	v_sub_u32_e32 v133, 0xff, v123
	v_sub_u32_e32 v152, 0xff, v151
	v_add_u32_e32 v154, 0x100, v153
	v_cmp_lt_u32_e64 s[10:11], 15, v111
	v_cmp_eq_u32_e64 s[12:13], 0, v111
	v_add_u32_e32 v157, 0xffffff00, v151
	v_add_u32_e32 v165, 0xe00, v164
	v_add_u32_e32 v166, 0x1c00, v164
	v_add_u32_e32 v167, 0x2a00, v164
	v_add_u32_e32 v170, 0x2200, v168
	v_add_u32_e32 v171, 0xe00, v169
	v_add_u32_e32 v172, 0x4400, v168
	v_add_u32_e32 v173, 0x1c00, v169
	v_add_u32_e32 v174, 0x6600, v168
	v_add_u32_e32 v175, 0x2a00, v169
	v_mov_b32_e32 v1, v132
	v_add_u32_e32 v109, 0x200, v108
	v_and_b32_e32 v178, -2, v7
	v_add_u32_e32 v119, 0xfffffe00, v108
	v_add_u32_e32 v180, s29, v176
	s_sub_i32 s40, 0, s33
	v_add_u32_e32 v181, 0x10900, v155
	v_sub_u32_e32 v182, 0, v123
	v_lshlrev_b32_e32 v136, 1, v116
	s_mov_b32 s42, 0x3f2aaaab
	v_mov_b32_e32 v183, 0x3ecc95a3
	s_mov_b32 s43, 0x3f317218
	s_mov_b32 s44, 0x7f800000
	s_mov_b32 s45, 0x33800000
	v_lshlrev_b32_e32 v138, 2, v122
	v_add_u32_e32 v185, v2, v118
	s_xor_b64 s[28:29], s[8:9], -1
	v_lshlrev_b32_e32 v114, 1, v4
	v_writelane_b32 v242, s47, 36
	s_add_i32 s0, s47, 0x1c70
	v_add_u32_e32 v186, v11, v13
	v_mov_b32_e32 v2, v115
	v_mov_b32_e32 v3, v115
	v_mov_b32_e32 v4, v115
	v_mov_b32_e32 v5, v115
	v_mov_b32_e32 v140, 0x3f317218
	v_mov_b32_e32 v187, 0x7f800000
	v_mov_b32_e32 v188, 0x7fc00000
	v_mov_b32_e32 v189, 0xff800000
	v_lshl_or_b32 v190, v184, 2, v6
	v_add_u32_e32 v191, v10, v13
	v_mov_b32_e32 v192, 0x7c
	v_writelane_b32 v242, s0, 38
	s_branch .LBB0_612

.LBB0_825:
	s_setprio 0
	s_waitcnt lgkmcnt(0)
	s_barrier
	s_waitcnt vmcnt(0)
	s_barrier
	s_mov_b64 s[0:1], exec
	v_readlane_b32 s2, v243, 5
	v_readlane_b32 s3, v243, 6
	s_and_b64 s[2:3], s[0:1], s[2:3]
	s_mov_b64 exec, s[2:3]
	s_cbranch_execz .LBB0_879
	v_readlane_b32 s2, v243, 2
	v_readlane_b32 s3, v243, 3
	s_mov_b32 s5, 0
	v_mov_b32_e32 v3, s2
	v_mov_b32_e32 v1, s3
	s_add_i32 s2, 0, 0x25c20
	v_readfirstlane_b32 s3, v1
	v_mov_b32_e32 v1, s2
	s_waitcnt vmcnt(0) expcnt(0) lgkmcnt(0)
	ds_read_b32 v2, v1
	s_add_i32 s2, 0, 0x25c24
	v_mov_b32_e32 v1, s2
	ds_read_b32 v1, v1
	v_readfirstlane_b32 s2, v3
	s_waitcnt lgkmcnt(1)
	v_cmp_eq_u32_e32 vcc, 0, v2
	s_cbranch_vccnz .LBB0_828
	v_readlane_b32 s4, v243, 4
	s_lshl_b32 s4, s4, 6
	s_mov_b32 s22, 1
	s_cbranch_execz .LBB0_829
	s_branch .LBB0_843

.LBB0_2009:
	s_add_i32 s3, 0, 0x25d38
	v_mov_b32_e32 v1, s3
	ds_read_b64 v[2:3], v1
	v_readfirstlane_b32 s3, v104
	s_cmpk_gt_i32 s54, 0xff
	s_waitcnt lgkmcnt(0)
	v_readfirstlane_b32 s4, v2
	v_readfirstlane_b32 s5, v3
	s_nop 0
	v_writelane_b32 v243, s4, 25
	s_nop 1
	v_writelane_b32 v243, s5, 26
	s_cbranch_scc1 .LBB0_2237
	v_readfirstlane_b32 s98, v0
	s_nop 3
	s_cmp_lt_u32 s98, 0x100
	s_cbranch_scc1 .Lp4prio1
	s_setprio 1
.Lp4prio1:
	s_or_b32 s42, s0, s33
	s_add_u32 s4, s2, 0x7400000
	s_addc_u32 s5, s1, 0
	s_add_u32 s36, s2, 0x17e00000
	s_addc_u32 s37, s1, 0
	s_add_u32 s0, s2, 0x300000
	v_writelane_b32 v242, s0, 41
	s_addc_u32 s0, s1, 0
	v_writelane_b32 v242, s0, 43
	s_add_u32 s0, s2, 0x1a200000
	v_writelane_b32 v243, s0, 29
	s_addc_u32 s0, s1, 0
	s_ashr_i32 s26, s3, 6
	v_writelane_b32 v242, s0, 25
	s_mul_i32 s0, s26, 0x2080
	s_add_i32 s43, s0, 0
	s_lshl_b32 s0, s54, 3
	s_add_i32 s15, s26, s0
	s_movk_i32 s0, 0x330
	v_cmp_gt_i32_e64 s[6:7], s0, v104
	v_readlane_b32 s14, v243, 23
	v_and_b32_e32 v1, 3, v104
	v_writelane_b32 v243, s6, 17
	s_add_i32 s43, s43, 0x14f00
	s_lshl_b32 s44, s14, 3
	v_writelane_b32 v243, s7, 18
	v_cmp_eq_u32_e64 s[6:7], 0, v1
	s_lshl_b32 s9, s26, 4
	s_cmp_gt_u32 s3, 63
	v_writelane_b32 v242, s6, 19
	v_and_b32_e32 v107, 63, v104
	v_ashrrev_i32_e32 v119, 2, v104
	v_writelane_b32 v242, s7, 20
	s_movk_i32 s6, 0x8ff
	v_cmp_lt_i32_e64 s[6:7], s6, v104
	s_movk_i32 s0, 0x70
	v_mul_lo_u32 v2, v119, s0
	v_writelane_b32 v242, s6, 13
	v_cmp_eq_u32_e64 s[12:13], 0, v107
	v_add_u32_e32 v106, 0, v2
	v_writelane_b32 v242, s7, 14
	s_cselect_b64 s[6:7], -1, 0
	s_cmp_lt_u32 s3, 64
	s_cselect_b64 s[10:11], -1, 0
	s_add_i32 s8, 0, 0x10700
	s_cmp_lg_u32 s42, 0
	v_lshlrev_b32_e32 v2, 1, v107
	v_writelane_b32 v243, s12, 31
	s_movk_i32 s3, 0xa0
	s_cselect_b64 s[84:85], -1, 0
	s_sub_i32 s45, 0, s33
	v_lshlrev_b32_e32 v108, 3, v1
	v_sub_u32_e32 v152, 0, v2
	v_writelane_b32 v243, s13, 32
	v_mad_u64_u32 v[2:3], s[12:13], v119, s3, v[106:107]
	v_lshlrev_b32_e32 v114, 4, v1
	s_add_u32 s38, s2, 0x2ce00000
	v_and_b32_e32 v1, 7, v104
	v_bfe_u32 v154, v104, 3, 3
	s_addc_u32 s39, s1, 0
	v_mul_u32_u24_e32 v3, 0x410, v1
	v_lshlrev_b32_e32 v7, 2, v154
	s_add_i32 s1, 0, 0x8800
	v_add3_u32 v155, s43, v3, v7
	v_add_u32_e32 v3, s1, v108
	s_lshl_b32 s2, s26, 5
	s_mul_i32 s1, s14, 0x88
	s_add_i32 s2, s2, 0
	s_add_i32 s1, s15, s1
	s_cmp_lt_i32 s1, s42
	s_cselect_b64 s[12:13], -1, 0
	s_cmp_ge_i32 s1, s33
	v_writelane_b32 v243, s15, 16
	s_cselect_b64 s[14:15], -1, 0
	s_and_b64 s[16:17], s[14:15], exec
	s_cselect_b32 s3, s45, s33
	s_add_i32 s18, s3, s1
	v_writelane_b32 v242, s10, 15
	s_mul_hi_i32 s1, s18, 0x30c30c31
	s_lshr_b32 s3, s1, 31
	v_writelane_b32 v242, s11, 16
	s_ashr_i32 s1, s1, 10
	v_readlane_b32 s16, v242, 27
	s_add_i32 s1, s1, s3
	v_readlane_b32 s17, v242, 28
	s_mul_i32 s3, s1, 0xffffeb00
	v_bfe_u32 v109, v104, 4, 2
	s_or_b64 s[14:15], s[16:17], s[14:15]
	s_add_i32 s35, s3, s18
	v_and_b32_e32 v113, 15, v104
	v_lshlrev_b32_e32 v118, 2, v109
	s_mov_b32 s3, 0xc600000
	s_and_b64 s[16:17], s[14:15], exec
	v_or_b32_e32 v147, s9, v113
	v_or_b32_e32 v7, s9, v118
	s_cselect_b32 s3, s3, 0x8000000
	s_lshl_b32 s9, s35, 1
	s_add_i32 s9, s9, 0x7fffe400
	s_lshl_b32 s16, s18, 5
	s_and_b32 s9, s9, 0x7fffffc0
	s_and_b32 s28, s16, 0x3e0
	s_and_b64 s[14:15], s[14:15], exec
	s_mov_b32 s16, 0xb800000
	s_mul_hi_i32 s14, s35, 0x92492493
	s_cselect_b32 s29, s16, 0x1000000
	s_add_i32 s14, s14, s35
	s_lshr_b32 s15, s14, 31
	s_ashr_i32 s14, s14, 7
	s_add_i32 s14, s14, s15
	s_lshl_b32 s30, s14, 6
	s_mulk_i32 s14, 0xe0
	s_sub_i32 s14, s35, s14
	s_lshl_b32 s34, s14, 5
	s_cmp_gt_i32 s26, -1
	s_cselect_b64 s[82:83], -1, 0
	s_cmp_gt_i32 s26, 0
	s_cselect_b64 s[14:15], -1, 0
	s_cmp_gt_i32 s26, 1
	s_cselect_b64 s[16:17], -1, 0
	s_cmp_gt_i32 s26, 2
	s_cselect_b64 s[18:19], -1, 0
	s_cmp_gt_i32 s26, 3
	s_cselect_b64 s[20:21], -1, 0
	s_cmp_gt_i32 s26, 4
	s_cselect_b64 s[22:23], -1, 0
	s_cmp_gt_i32 s26, 5
	s_cselect_b64 s[24:25], -1, 0
	s_cmp_gt_i32 s26, 6
	s_cselect_b64 s[26:27], -1, 0
	s_and_b64 s[12:13], s[84:85], s[12:13]
	v_writelane_b32 v242, s12, 17
	v_lshl_add_u32 v11, v7, 1, 0
	v_or_b32_e32 v7, 2, v118
	v_writelane_b32 v242, s13, 18
	v_cmp_gt_i32_e64 s[12:13], v118, v147
	v_bfe_u32 v5, v104, 2, 2
	v_lshlrev_b32_e32 v112, 3, v109
	v_writelane_b32 v243, s12, 33
	v_lshlrev_b32_e32 v6, 2, v107
	v_add_u32_e32 v149, s8, v6
	v_writelane_b32 v243, s13, 34
	v_cmp_lt_i32_e64 s[12:13], v118, v147
	v_add_u32_e32 v151, 0, v6
	v_and_b32_e32 v159, 28, v6
	v_writelane_b32 v243, s12, 35
	v_or_b32_e32 v6, v112, v5
	s_cmpk_lt_i32 s35, 0xe00
	v_writelane_b32 v243, s13, 36
	v_cmp_gt_i32_e64 s[12:13], v7, v147
	v_or_b32_e32 v7, 3, v118
	v_or_b32_e32 v5, v118, v5
	v_writelane_b32 v243, s12, 37
	v_mad_u32_u24 v160, v5, s0, v3
	v_mul_u32_u24_e32 v5, 0x110, v6
	v_writelane_b32 v243, s13, 38
	v_cmp_gt_i32_e64 s[12:13], v7, v147
	v_or_b32_e32 v7, 16, v118
	v_mad_u32_u24 v165, v6, s0, v3
	v_writelane_b32 v243, s12, 39
	s_movk_i32 s0, 0x400
	s_cselect_b32 s3, s29, s3
	v_writelane_b32 v243, s13, 40
	v_cmp_gt_i32_e64 s[12:13], v7, v147
	v_or_b32_e32 v7, 17, v118
	v_add3_u32 v164, s2, v108, v5
	v_writelane_b32 v243, s12, 41
	s_cselect_b32 s2, s0, 0xe00
	s_cselect_b32 s0, s30, s9
	v_writelane_b32 v243, s13, 42
	v_cmp_gt_i32_e64 s[12:13], v7, v147
	v_or_b32_e32 v7, 18, v118
	s_cselect_b32 s9, s34, s28
	v_writelane_b32 v243, s12, 43
	v_mov_b32_e32 v111, 0
	v_and_b32_e32 v110, 48, v104
	v_writelane_b32 v243, s13, 44
	v_cmp_gt_i32_e64 s[12:13], v7, v147
	v_or_b32_e32 v7, 19, v118
	v_lshlrev_b32_e32 v4, 3, v1
	v_writelane_b32 v243, s12, 45
	v_or_b32_e32 v156, 8, v154
	v_lshl_add_u64 v[116:117], s[36:37], 0, v[110:111]
	v_writelane_b32 v243, s13, 46
	v_cmp_gt_i32_e64 s[12:13], v7, v147
	v_or_b32_e32 v7, 32, v118
	v_add_u32_e32 v10, 0, v110
	v_writelane_b32 v243, s12, 47
	v_lshlrev_b32_e32 v110, 4, v1
	v_or_b32_e32 v1, s9, v154
	v_writelane_b32 v243, s13, 48
	v_cmp_gt_i32_e64 s[12:13], v7, v147
	v_or_b32_e32 v7, 33, v118
	v_or_b32_e32 v157, 16, v154
	v_writelane_b32 v243, s12, 49
	v_or_b32_e32 v158, 24, v154
	v_lshlrev_b32_e32 v172, 2, v104
	v_writelane_b32 v243, s13, 50
	v_cmp_gt_i32_e64 s[12:13], v7, v147
	v_or_b32_e32 v7, 34, v118
	v_add_u32_e32 v3, 0, v172
	v_writelane_b32 v243, s12, 51
	v_add_u32_e32 v3, 0x12b00, v3
	v_and_b32_e32 v12, 0x7f, v104
	v_writelane_b32 v243, s13, 52
	v_cmp_gt_i32_e64 s[12:13], v7, v147
	v_or_b32_e32 v7, 35, v118
	v_mul_u32_u24_e32 v13, 0x110, v113
	v_writelane_b32 v243, s12, 53
	v_or_b32_e32 v128, 0xffffff00, v12
	v_mov_b32_e32 v115, v111
	v_writelane_b32 v243, s13, 54
	v_cmp_gt_i32_e64 s[12:13], v7, v147
	v_or_b32_e32 v7, 48, v118
	v_mbcnt_hi_u32_b32 v180, -1, v212
	v_writelane_b32 v243, s12, 55
	s_mov_b32 s31, 0
	v_sub_u32_e32 v129, 0xff, v119
	v_writelane_b32 v243, s13, 56
	v_cmp_gt_i32_e64 s[12:13], v7, v147
	v_or_b32_e32 v7, 49, v118
	v_sub_u32_e32 v148, 0xff, v147
	v_writelane_b32 v243, s12, 57
	s_movk_i32 s52, 0x100
	v_add_u32_e32 v150, 0x100, v149
	v_writelane_b32 v243, s13, 58
	v_cmp_gt_i32_e64 s[12:13], v7, v147
	v_or_b32_e32 v7, 50, v118
	v_cmp_lt_u32_e64 s[10:11], 15, v107
	v_writelane_b32 v243, s12, 59
	v_add_u32_e32 v153, 0xffffff00, v147
	v_add_u32_e32 v161, 0xe00, v160
	v_writelane_b32 v243, s13, 60
	v_cmp_gt_i32_e64 s[12:13], v7, v147
	v_or_b32_e32 v7, 51, v118
	v_add_u32_e32 v162, 0x1c00, v160
	v_writelane_b32 v243, s12, 61
	v_add_u32_e32 v163, 0x2a00, v160
	v_add_u32_e32 v166, 0x2200, v164
	v_writelane_b32 v243, s13, 62
	v_cmp_gt_i32_e64 s[12:13], v7, v147
	v_or_b32_e32 v7, 64, v118
	v_add_u32_e32 v167, 0xe00, v165
	v_writelane_b32 v243, s12, 63
	v_writelane_b32 v243, s36, 27
	v_add_u32_e32 v168, 0x4400, v164
	v_writelane_b32 v242, s13, 0
	v_cmp_gt_i32_e64 s[12:13], v7, v147
	v_or_b32_e32 v7, 0x41, v118
	v_writelane_b32 v243, s37, 28
	v_writelane_b32 v242, s12, 1
	v_add_u32_e32 v169, 0x1c00, v165
	v_add_u32_e32 v170, 0x6600, v164
	v_writelane_b32 v242, s13, 2
	v_cmp_gt_i32_e64 s[12:13], v7, v147
	v_or_b32_e32 v7, 0x42, v118
	v_add_u32_e32 v171, 0x2a00, v165
	v_writelane_b32 v242, s12, 3
	v_add_u32_e32 v105, 0x200, v104
	v_lshl_add_u64 v[130:131], s[36:37], 0, v[114:115]
	v_writelane_b32 v242, s13, 4
	v_cmp_gt_i32_e64 s[12:13], v7, v147
	v_or_b32_e32 v7, 0x43, v118
	v_add_u32_e32 v115, 0xfffffe00, v104
	v_writelane_b32 v242, s12, 5
	v_add_u32_e32 v176, s8, v172
	v_add_u32_e32 v177, 0x10900, v151
	v_writelane_b32 v242, s13, 6
	v_cmp_gt_i32_e64 s[12:13], v7, v147
	v_or_b32_e32 v7, 0x50, v118
	v_sub_u32_e32 v178, 0, v119
	v_writelane_b32 v242, s12, 11
	v_lshlrev_b32_e32 v132, 1, v112
	s_mov_b32 s47, 0x3f2aaaab
	v_writelane_b32 v242, s13, 12
	v_cmp_gt_i32_e64 s[12:13], v7, v147
	v_or_b32_e32 v7, 0x51, v118
	v_mov_b32_e32 v179, 0x3ecc95a3
	v_writelane_b32 v242, s12, 36
	s_mov_b32 s48, 0x3f317218
	s_mov_b32 s49, 0x7f800000
	v_writelane_b32 v242, s13, 37
	v_cmp_gt_i32_e64 s[12:13], v7, v147
	v_or_b32_e32 v7, 0x52, v118
	v_cmp_gt_i32_e64 s[60:61], v7, v147
	v_writelane_b32 v242, s12, 7
	v_or_b32_e32 v7, 0x53, v118
	v_cmp_gt_i32_e64 s[62:63], v7, v147
	v_writelane_b32 v242, s13, 8
	v_or_b32_e32 v7, 0x60, v118
	s_mov_b32 s12, 0xe00000
	v_cmp_gt_i32_e64 s[64:65], v7, v147
	v_or_b32_e32 v7, 0x61, v118
	s_cselect_b32 s12, s12, 0x700000
	s_add_u32 s3, s38, s3
	v_cmp_gt_i32_e64 s[66:67], v7, v147
	v_or_b32_e32 v7, 0x62, v118
	s_addc_u32 s13, s39, 0
	s_mul_hi_i32 s28, s12, s1
	s_mul_i32 s12, s12, s1
	v_cmp_gt_i32_e64 s[68:69], v7, v147
	v_or_b32_e32 v7, 0x63, v118
	s_add_u32 s3, s3, s12
	v_cmp_gt_i32_e64 s[70:71], v7, v147
	v_or_b32_e32 v7, 0x70, v118
	s_addc_u32 s12, s13, s28
	s_ashr_i32 s1, s0, 31
	v_cmp_gt_i32_e64 s[72:73], v7, v147
	v_or_b32_e32 v7, 0x71, v118
	s_lshl_b64 s[0:1], s[0:1], 1
	v_cmp_gt_i32_e64 s[74:75], v7, v147
	v_or_b32_e32 v7, 0x72, v118
	s_add_u32 s0, s3, s0
	v_cmp_gt_i32_e64 s[76:77], v7, v147
	v_or_b32_e32 v7, 0x73, v118
	s_addc_u32 s1, s12, s1
	v_cmp_gt_i32_e64 s[78:79], v7, v147
	v_lshl_add_u64 v[6:7], s[0:1], 0, v[110:111]
	v_mad_i64_i32 v[8:9], s[0:1], s2, v1, 0
	v_or_b32_e32 v1, s9, v156
	v_lshl_add_u64 v[120:121], v[8:9], 1, v[6:7]
	v_mad_i64_i32 v[8:9], s[0:1], s2, v1, 0
	v_or_b32_e32 v1, s9, v157
	v_lshl_add_u64 v[122:123], v[8:9], 1, v[6:7]
	v_mad_i64_i32 v[8:9], s[0:1], s2, v1, 0
	v_or_b32_e32 v1, s9, v158
	v_lshl_add_u64 v[124:125], v[8:9], 1, v[6:7]
	v_mad_i64_i32 v[8:9], s[0:1], s2, v1, 0
	v_max_i32_e32 v1, 0x700, v104
	v_sub_u32_e32 v1, v1, v104
	v_add_u32_e32 v1, 0x1ff, v1
	v_lshl_add_u64 v[126:127], v[8:9], 1, v[6:7]
	v_lshlrev_b32_e32 v8, 2, v1
	s_movk_i32 s0, 0xdff
	v_and_b32_e32 v8, 0xfffff800, v8
	v_lshrrev_b32_e32 v5, 9, v1
	v_cmp_lt_u32_e32 vcc, s0, v1
	v_cmp_gt_u32_e64 s[0:1], 2.0, v1
	v_add_u32_e32 v1, v3, v8
	v_writelane_b32 v242, s38, 29
	v_add_u32_e32 v6, 1, v5
	v_add_u32_e32 v5, -1, v5
	v_cmp_ge_u32_e64 s[2:3], v1, v3
	v_writelane_b32 v242, s39, 39
	s_and_b64 s[0:1], s[2:3], s[0:1]
	v_cmp_lt_u32_e64 s[2:3], 1, v5
	v_lshrrev_b32_e32 v7, 1, v5
	v_and_b32_e32 v5, 2, v5
	v_writelane_b32 v242, s2, 45
	v_and_b32_e32 v3, 0xfffffe, v6
	s_and_b64 s[0:1], vcc, s[0:1]
	v_writelane_b32 v242, s3, 46
	v_cmp_eq_u32_e64 s[2:3], 0, v5
	v_lshl_add_u32 v173, v3, 9, v104
	v_add_u32_e32 v7, 1, v7
	v_writelane_b32 v242, s2, 47
	v_mov_b32_e32 v1, v128
	v_and_b32_e32 v174, -2, v7
	v_writelane_b32 v242, s3, 48
	v_cmp_ne_u32_e64 s[2:3], v6, v3
	v_lshl_add_u32 v3, v104, 4, 0
	v_add_u32_e32 v175, 0xc000, v3
	v_writelane_b32 v242, s2, 49
	v_bfrev_b32_e32 v6, 0.5
	s_sub_i32 s46, 0, s44
	v_writelane_b32 v242, s3, 50
	v_writelane_b32 v242, s0, 51
	s_mov_b32 s50, 0x33800000
	v_lshlrev_b32_e32 v134, 2, v118
	v_writelane_b32 v242, s1, 52
	s_add_i32 s0, 0, 0x25de0
	v_writelane_b32 v243, s0, 14
	s_add_i32 s0, 0, 0x25db8
	v_writelane_b32 v242, s0, 23
	s_add_i32 s0, 0, 0x25dd0
	v_writelane_b32 v242, s0, 21
	s_add_i32 s0, 0, 0x25da8
	v_writelane_b32 v243, s0, 19
	s_add_i32 s0, 0, 0x25dd8
	v_writelane_b32 v243, s0, 20
	s_add_i32 s0, 0, 0x25db0
	v_writelane_b32 v242, s0, 10
	s_add_i32 s0, s43, 0x820
	v_writelane_b32 v242, s0, 31
	s_add_i32 s0, s43, 0xc30
	v_writelane_b32 v242, s0, 33
	s_add_i32 s0, s43, 0x1040
	v_writelane_b32 v242, s0, 34
	s_add_i32 s0, s43, 0x1450
	v_writelane_b32 v242, s0, 35
	s_add_i32 s0, s43, 0x1860
	v_add_u32_e32 v181, v2, v114
	s_xor_b64 s[28:29], s[84:85], -1
	v_lshlrev_b32_e32 v110, 1, v4
	v_writelane_b32 v242, s0, 38
	s_add_i32 s0, s43, 0x1c70
	v_add_u32_e32 v182, v11, v13
	v_mov_b32_e32 v2, v111
	v_mov_b32_e32 v3, v111
	v_mov_b32_e32 v4, v111
	v_mov_b32_e32 v5, v111
	v_mov_b32_e32 v136, 0x3f317218
	v_mov_b32_e32 v183, 0x7f800000
	v_mov_b32_e32 v184, 0x7fc00000
	v_mov_b32_e32 v185, 0xff800000
	v_lshl_or_b32 v186, v180, 2, v6
	v_add_u32_e32 v187, v10, v13
	v_mov_b32_e32 v188, 0x7c
	v_writelane_b32 v242, s0, 24
	s_branch .LBB0_2012

.LBB0_3626:
	s_or_b64 exec, exec, s[0:1]
	s_load_dwordx2 s[0:1], s[80:81], 0xf0
	v_mov_b32_e32 v104, v0
	s_waitcnt lgkmcnt(0)
	s_barrier
	v_mov_b32_e32 v1, s0
	v_mov_b32_e32 v2, s1
	s_add_i32 s0, 0, 0x25d38
	v_readfirstlane_b32 s2, v2
	v_mov_b32_e32 v2, s79
	v_mov_b32_e32 v4, s77
	v_mov_b32_e32 v5, s78
	v_mov_b32_e32 v2, s0
	ds_read_b64 v[2:3], v2
	v_readfirstlane_b32 s52, v4
	v_readfirstlane_b32 s3, v1
	v_readfirstlane_b32 s53, v5
	s_mov_b32 s35, 0
	s_waitcnt lgkmcnt(0)
	v_readfirstlane_b32 s0, v2
	v_readfirstlane_b32 s1, v3
	s_cmpk_gt_i32 s52, 0xff
	v_writelane_b32 v243, s0, 27
	v_readfirstlane_b32 s10, v104
	s_nop 0
	v_writelane_b32 v243, s1, 28
	s_cbranch_scc1 .LBB0_3854
	v_readfirstlane_b32 s98, v0
	s_nop 3
	s_cmp_lt_u32 s98, 0x100
	s_cbranch_scc1 .Lp4prio2
	s_setprio 1
.Lp4prio2:
	s_add_u32 s4, s3, 0x7400000
	s_addc_u32 s5, s2, 0
	s_add_u32 s44, s3, 0x17e00000
	s_addc_u32 s45, s2, 0
	s_add_u32 s0, s3, 0x300000
	v_writelane_b32 v242, s0, 45
	s_addc_u32 s0, s2, 0
	v_writelane_b32 v242, s0, 47
	s_add_u32 s0, s3, 0x1a200000
	v_writelane_b32 v243, s0, 16
	s_addc_u32 s0, s2, 0
	s_ashr_i32 s28, s10, 6
	v_writelane_b32 v243, s0, 17
	s_mul_i32 s0, s28, 0x2080
	s_add_i32 s0, s0, 0
	s_add_i32 s48, s0, 0x14f00
	s_lshl_b32 s0, s52, 3
	s_add_i32 s46, s28, s0
	s_lshl_b32 s33, s53, 3
	s_cmpk_eq_i32 s53, 0x100
	s_cselect_b64 s[8:9], -1, 0
	s_and_b64 s[0:1], s[8:9], exec
	s_movk_i32 s1, 0x330
	v_cmp_gt_i32_e64 s[6:7], s1, v104
	v_and_b32_e32 v1, 3, v104
	s_cselect_b32 s16, 0x4800, 0
	v_writelane_b32 v242, s6, 13
	s_cselect_b32 s0, 3, 0
	s_lshl_b32 s17, s28, 4
	v_writelane_b32 v242, s7, 14
	v_cmp_eq_u32_e64 s[6:7], 0, v1
	v_ashrrev_i32_e32 v119, 2, v104
	s_movk_i32 s1, 0x70
	v_writelane_b32 v242, s6, 15
	s_cmp_gt_u32 s10, 63
	v_and_b32_e32 v107, 63, v104
	v_writelane_b32 v242, s7, 16
	s_movk_i32 s6, 0x8ff
	v_cmp_lt_i32_e64 s[6:7], s6, v104
	v_mul_lo_u32 v2, v119, s1
	v_add_u32_e32 v106, 0, v2
	v_writelane_b32 v242, s6, 17
	v_lshlrev_b32_e32 v2, 1, v107
	s_movk_i32 s14, 0xa0
	v_writelane_b32 v242, s7, 18
	s_cselect_b64 s[6:7], -1, 0
	s_cmp_lt_u32 s10, 64
	s_cselect_b64 s[10:11], -1, 0
	s_add_i32 s29, 0, 0x10700
	v_lshlrev_b32_e32 v108, 3, v1
	v_sub_u32_e32 v152, 0, v2
	v_mad_u64_u32 v[2:3], s[14:15], v119, s14, v[106:107]
	v_lshlrev_b32_e32 v114, 4, v1
	s_add_u32 s47, s3, 0x2ce00000
	v_and_b32_e32 v1, 7, v104
	v_bfe_u32 v154, v104, 3, 3
	s_addc_u32 s50, s2, 0
	v_mul_u32_u24_e32 v3, 0x410, v1
	v_lshlrev_b32_e32 v6, 2, v154
	s_add_i32 s2, 0, 0x8800
	v_add3_u32 v155, s48, v3, v6
	v_add_u32_e32 v3, s2, v108
	s_lshl_b32 s3, s28, 5
	s_mul_i32 s2, s53, 0x88
	s_add_i32 s3, s3, 0
	s_add_i32 s20, s46, s2
	s_cmp_lt_i32 s20, s16
	v_bfe_u32 v109, v104, 4, 2
	s_cselect_b64 s[42:43], -1, 0
	s_cmp_ge_i32 s20, s16
	v_and_b32_e32 v113, 15, v104
	v_lshlrev_b32_e32 v118, 2, v109
	s_cselect_b64 s[14:15], -1, 0
	v_or_b32_e32 v147, s17, v113
	v_or_b32_e32 v8, s17, v118
	s_and_b64 s[16:17], s[8:9], s[14:15]
	s_and_b64 s[16:17], s[16:17], exec
	s_cselect_b32 s2, 0xffffb800, 0
	s_add_i32 s21, s2, s20
	s_bfe_i32 s2, s0, 0x10000
	s_and_b32 s16, s0, 1
	v_writelane_b32 v242, s10, 41
	s_bitcmp1_b32 s0, 0
	s_cselect_b64 s[18:19], -1, 0
	v_writelane_b32 v242, s11, 42
	s_cmp_eq_u32 s16, 0
	v_writelane_b32 v242, s18, 31
	s_cselect_b64 s[16:17], -1, 0
	s_mul_hi_i32 s22, s21, 0x30c30c31
	v_writelane_b32 v242, s19, 32
	s_and_b64 s[18:19], s[16:17], exec
	s_mov_b32 s23, 0xc600000
	s_mov_b32 s18, 0xb800000
	s_cselect_b32 s34, s23, 0x8000000
	s_cselect_b32 s54, s18, 0x1000000
	s_or_b64 s[14:15], s[16:17], s[14:15]
	s_lshr_b32 s16, s22, 31
	s_ashr_i32 s30, s22, 10
	s_add_i32 s30, s30, s16
	s_mul_i32 s16, s30, 0xffffeb00
	s_add_i32 s41, s16, s21
	s_and_b64 s[16:17], s[14:15], exec
	s_cselect_b32 s31, s23, 0x8000000
	s_lshl_b32 s16, s41, 1
	s_add_i32 s16, s16, 0x7fffe400
	s_and_b32 s36, s16, 0x7fffffc0
	s_lshl_b32 s16, s20, 5
	s_and_b32 s37, s16, 0x3e0
	s_mul_hi_i32 s19, s41, 0x92492493
	s_and_b64 s[14:15], s[14:15], exec
	s_cselect_b32 s38, s18, 0x1000000
	s_add_i32 s19, s19, s41
	s_lshr_b32 s14, s19, 31
	s_ashr_i32 s15, s19, 7
	s_add_i32 s14, s15, s14
	s_mul_i32 s15, s14, 0xe0
	s_lshl_b32 s39, s14, 6
	s_sub_i32 s14, s41, s15
	s_lshl_b32 s40, s14, 5
	s_cmp_gt_i32 s28, -1
	s_cselect_b64 s[84:85], -1, 0
	s_cmp_gt_i32 s28, 0
	s_cselect_b64 s[14:15], -1, 0
	s_cmp_gt_i32 s28, 1
	s_cselect_b64 s[16:17], -1, 0
	s_cmp_gt_i32 s28, 2
	s_cselect_b64 s[18:19], -1, 0
	s_cmp_gt_i32 s28, 3
	s_cselect_b64 s[20:21], -1, 0
	s_cmp_gt_i32 s28, 4
	s_cselect_b64 s[22:23], -1, 0
	s_cmp_gt_i32 s28, 5
	s_cselect_b64 s[24:25], -1, 0
	s_cmp_gt_i32 s28, 6
	s_cselect_b64 s[26:27], -1, 0
	s_and_b64 s[42:43], s[8:9], s[42:43]
	v_writelane_b32 v242, s42, 43
	v_lshl_add_u32 v12, v8, 1, 0
	v_or_b32_e32 v8, 2, v118
	v_writelane_b32 v242, s43, 44
	v_cmp_gt_i32_e64 s[42:43], v118, v147
	v_bfe_u32 v5, v104, 2, 2
	v_lshlrev_b32_e32 v112, 3, v109
	v_writelane_b32 v243, s42, 31
	v_lshlrev_b32_e32 v7, 2, v107
	v_add_u32_e32 v149, s29, v7
	v_writelane_b32 v243, s43, 32
	v_cmp_lt_i32_e64 s[42:43], v118, v147
	v_add_u32_e32 v151, 0, v7
	v_and_b32_e32 v159, 28, v7
	v_writelane_b32 v243, s42, 33
	v_or_b32_e32 v7, v112, v5
	v_or_b32_e32 v5, v118, v5
	v_writelane_b32 v243, s43, 34
	v_cmp_gt_i32_e64 s[42:43], v8, v147
	v_or_b32_e32 v8, 3, v118
	s_cmpk_lt_i32 s41, 0xe00
	v_writelane_b32 v243, s42, 35
	v_mad_u32_u24 v160, v5, s1, v3
	v_mul_u32_u24_e32 v5, 0x110, v7
	v_writelane_b32 v243, s43, 36
	v_cmp_gt_i32_e64 s[42:43], v8, v147
	v_or_b32_e32 v8, 16, v118
	v_add3_u32 v164, s3, v108, v5
	v_writelane_b32 v243, s42, 37
	s_cselect_b32 s3, s40, s37
	s_mov_b32 s37, 0xe00000
	v_writelane_b32 v243, s43, 38
	v_cmp_gt_i32_e64 s[42:43], v8, v147
	v_or_b32_e32 v8, 17, v118
	v_mad_u32_u24 v165, v7, s1, v3
	v_writelane_b32 v243, s42, 39
	s_movk_i32 s1, 0x400
	s_cselect_b32 s31, s38, s31
	v_writelane_b32 v243, s43, 40
	v_cmp_gt_i32_e64 s[42:43], v8, v147
	v_or_b32_e32 v8, 18, v118
	s_cselect_b32 s37, s37, 0x700000
	v_writelane_b32 v243, s42, 41
	s_cselect_b32 s1, s1, 0xe00
	s_cselect_b32 s36, s39, s36
	v_writelane_b32 v243, s43, 42
	v_cmp_gt_i32_e64 s[42:43], v8, v147
	v_or_b32_e32 v8, 19, v118
	s_mul_hi_i32 s38, s37, s30
	v_writelane_b32 v243, s42, 43
	s_mul_i32 s37, s37, s30
	s_add_u32 s30, s47, s31
	v_writelane_b32 v243, s43, 44
	v_cmp_gt_i32_e64 s[42:43], v8, v147
	v_or_b32_e32 v8, 32, v118
	s_addc_u32 s31, s50, 0
	v_writelane_b32 v243, s42, 45
	s_add_u32 s39, s30, s37
	s_addc_u32 s38, s31, s38
	v_writelane_b32 v243, s43, 46
	v_cmp_gt_i32_e64 s[42:43], v8, v147
	v_or_b32_e32 v8, 33, v118
	s_ashr_i32 s37, s36, 31
	v_writelane_b32 v243, s42, 47
	s_lshl_b64 s[30:31], s[36:37], 1
	v_mov_b32_e32 v111, 0
	v_writelane_b32 v243, s43, 48
	v_cmp_gt_i32_e64 s[42:43], v8, v147
	v_or_b32_e32 v8, 34, v118
	v_and_b32_e32 v110, 48, v104
	v_writelane_b32 v243, s42, 49
	s_add_u32 s30, s39, s30
	v_lshlrev_b32_e32 v4, 3, v1
	v_writelane_b32 v243, s43, 50
	v_cmp_gt_i32_e64 s[42:43], v8, v147
	v_or_b32_e32 v8, 35, v118
	v_or_b32_e32 v156, 8, v154
	v_writelane_b32 v243, s42, 51
	v_lshl_add_u64 v[116:117], s[44:45], 0, v[110:111]
	v_add_u32_e32 v6, 0, v110
	v_writelane_b32 v243, s43, 52
	v_cmp_gt_i32_e64 s[42:43], v8, v147
	v_or_b32_e32 v8, 48, v118
	s_addc_u32 s31, s38, s31
	v_writelane_b32 v243, s42, 53
	v_lshlrev_b32_e32 v110, 4, v1
	v_or_b32_e32 v1, s3, v154
	v_writelane_b32 v243, s43, 54
	v_cmp_gt_i32_e64 s[42:43], v8, v147
	v_or_b32_e32 v8, 49, v118
	v_or_b32_e32 v157, 16, v154
	v_writelane_b32 v243, s42, 55
	v_or_b32_e32 v158, 24, v154
	s_lshr_b32 s0, s0, 1
	v_writelane_b32 v243, s43, 56
	v_cmp_gt_i32_e64 s[42:43], v8, v147
	v_or_b32_e32 v8, 50, v118
	v_lshlrev_b32_e32 v172, 2, v104
	v_writelane_b32 v243, s42, 57
	v_add_u32_e32 v3, 0, v172
	v_add_u32_e32 v3, 0x12b00, v3
	v_writelane_b32 v243, s43, 58
	v_cmp_gt_i32_e64 s[42:43], v8, v147
	v_or_b32_e32 v8, 51, v118
	v_and_b32_e32 v13, 0x7f, v104
	v_writelane_b32 v243, s42, 59
	v_mul_u32_u24_e32 v14, 0x110, v113
	v_or_b32_e32 v128, 0xffffff00, v13
	v_writelane_b32 v243, s43, 60
	v_cmp_gt_i32_e64 s[42:43], v8, v147
	v_or_b32_e32 v8, 64, v118
	v_mov_b32_e32 v115, v111
	v_writelane_b32 v243, s42, 61
	v_mbcnt_hi_u32_b32 v180, -1, v212
	s_movk_i32 s49, 0x100
	v_writelane_b32 v243, s43, 62
	v_cmp_gt_i32_e64 s[42:43], v8, v147
	v_or_b32_e32 v8, 0x41, v118
	v_sub_u32_e32 v129, 0xff, v119
	v_writelane_b32 v243, s42, 63
	v_writelane_b32 v243, s34, 14
	s_mov_b32 s55, s35
	v_writelane_b32 v242, s43, 0
	v_cmp_gt_i32_e64 s[42:43], v8, v147
	v_or_b32_e32 v8, 0x42, v118
	v_writelane_b32 v243, s35, 15
	v_writelane_b32 v242, s42, 1
	v_sub_u32_e32 v148, 0xff, v147
	v_add_u32_e32 v150, 0x100, v149
	v_writelane_b32 v242, s43, 2
	v_cmp_gt_i32_e64 s[42:43], v8, v147
	v_or_b32_e32 v8, 0x43, v118
	v_cmp_lt_u32_e64 s[10:11], 15, v107
	v_writelane_b32 v242, s42, 3
	v_cmp_eq_u32_e64 s[12:13], 0, v107
	v_add_u32_e32 v153, 0xffffff00, v147
	v_writelane_b32 v242, s43, 4
	v_cmp_gt_i32_e64 s[42:43], v8, v147
	v_or_b32_e32 v8, 0x50, v118
	v_add_u32_e32 v161, 0xe00, v160
	v_writelane_b32 v242, s42, 5
	v_add_u32_e32 v162, 0x1c00, v160
	v_add_u32_e32 v163, 0x2a00, v160
	v_writelane_b32 v242, s43, 6
	v_cmp_gt_i32_e64 s[42:43], v8, v147
	v_or_b32_e32 v8, 0x51, v118
	v_cmp_gt_i32_e64 s[58:59], v8, v147
	v_or_b32_e32 v8, 0x52, v118
	v_cmp_gt_i32_e64 s[60:61], v8, v147
	v_or_b32_e32 v8, 0x53, v118
	v_cmp_gt_i32_e64 s[62:63], v8, v147
	v_or_b32_e32 v8, 0x60, v118
	v_cmp_gt_i32_e64 s[64:65], v8, v147
	v_or_b32_e32 v8, 0x61, v118
	v_cmp_gt_i32_e64 s[66:67], v8, v147
	v_or_b32_e32 v8, 0x62, v118
	v_cmp_gt_i32_e64 s[68:69], v8, v147
	v_or_b32_e32 v8, 0x63, v118
	v_cmp_gt_i32_e64 s[70:71], v8, v147
	v_or_b32_e32 v8, 0x70, v118
	v_cmp_gt_i32_e64 s[72:73], v8, v147
	v_or_b32_e32 v8, 0x71, v118
	v_cmp_gt_i32_e64 s[74:75], v8, v147
	v_or_b32_e32 v8, 0x72, v118
	v_cmp_gt_i32_e64 s[76:77], v8, v147
	v_or_b32_e32 v8, 0x73, v118
	v_writelane_b32 v242, s42, 11
	v_cmp_gt_i32_e64 s[78:79], v8, v147
	v_lshl_add_u64 v[8:9], s[30:31], 0, v[110:111]
	v_mad_i64_i32 v[10:11], s[30:31], s1, v1, 0
	v_or_b32_e32 v1, s3, v156
	v_writelane_b32 v242, s43, 12
	v_lshl_add_u64 v[120:121], v[10:11], 1, v[8:9]
	v_mad_i64_i32 v[10:11], s[30:31], s1, v1, 0
	v_or_b32_e32 v1, s3, v157
	v_writelane_b32 v242, s47, 9
	v_lshl_add_u64 v[122:123], v[10:11], 1, v[8:9]
	v_mad_i64_i32 v[10:11], s[30:31], s1, v1, 0
	v_or_b32_e32 v1, s3, v158
	v_writelane_b32 v242, s50, 30
	v_lshl_add_u64 v[124:125], v[10:11], 1, v[8:9]
	v_mad_i64_i32 v[10:11], s[30:31], s1, v1, 0
	s_lshl_b32 s1, s46, 5
	v_writelane_b32 v242, s46, 19
	s_and_b32 s1, s1, 0x3e0
	v_max_i32_e32 v1, 0x700, v104
	v_writelane_b32 v242, s1, 36
	v_sub_u32_e32 v1, v1, v104
	v_writelane_b32 v242, s54, 39
	s_and_b32 s1, s2, 3
	v_add_u32_e32 v1, 0x1ff, v1
	v_lshl_add_u64 v[126:127], v[10:11], 1, v[8:9]
	v_writelane_b32 v242, s55, 40
	s_lshl_b32 s0, s0, s1
	v_lshlrev_b32_e32 v9, 2, v1
	v_writelane_b32 v242, s0, 33
	s_movk_i32 s0, 0xdff
	v_and_b32_e32 v9, 0xfffff800, v9
	v_lshrrev_b32_e32 v5, 9, v1
	v_cmp_lt_u32_e32 vcc, s0, v1
	v_cmp_gt_u32_e64 s[0:1], 2.0, v1
	v_add_u32_e32 v1, v3, v9
	v_add_u32_e32 v7, 1, v5
	v_add_u32_e32 v5, -1, v5
	v_cmp_ge_u32_e64 s[2:3], v1, v3
	s_and_b64 s[0:1], s[2:3], s[0:1]
	v_cmp_lt_u32_e64 s[2:3], 1, v5
	v_lshrrev_b32_e32 v8, 1, v5
	v_and_b32_e32 v5, 2, v5
	v_writelane_b32 v242, s2, 53
	v_and_b32_e32 v3, 0xfffffe, v7
	s_and_b64 s[0:1], vcc, s[0:1]
	v_writelane_b32 v242, s3, 54
	v_cmp_eq_u32_e64 s[2:3], 0, v5
	s_lshl_b32 s43, s53, 4
	v_lshl_add_u32 v173, v3, 9, v104
	v_writelane_b32 v242, s2, 55
	v_add_u32_e32 v8, 1, v8
	v_add_u32_e32 v166, 0x2200, v164
	v_writelane_b32 v242, s3, 56
	v_cmp_ne_u32_e64 s[2:3], v7, v3
	v_lshl_add_u32 v3, v104, 4, 0
	v_add_u32_e32 v175, 0xc000, v3
	v_writelane_b32 v242, s2, 57
	v_bfrev_b32_e32 v7, 0.5
	v_add_u32_e32 v167, 0xe00, v165
	v_writelane_b32 v242, s3, 58
	v_writelane_b32 v242, s0, 49
	v_add_u32_e32 v168, 0x4400, v164
	v_add_u32_e32 v169, 0x1c00, v165
	v_writelane_b32 v242, s1, 50
	v_writelane_b32 v242, s44, 25
	s_sub_i32 s0, 0, s43
	s_lshl_b32 s1, s28, 1
	v_writelane_b32 v242, s45, 26
	v_writelane_b32 v242, s0, 23
	s_lshl_b32 s0, s52, 4
	s_add_i32 s0, s0, s1
	s_add_i32 s0, s0, 0x7fffe400
	v_writelane_b32 v242, s0, 51
	s_add_i32 s0, 0, 0x25de0
	v_writelane_b32 v242, s0, 21
	s_add_i32 s0, 0, 0x25db8
	v_writelane_b32 v243, s0, 19
	s_add_i32 s0, 0, 0x25dd0
	v_writelane_b32 v243, s0, 20
	s_add_i32 s0, 0, 0x25da8
	v_writelane_b32 v242, s0, 10
	s_add_i32 s0, 0, 0x25dd8
	v_writelane_b32 v243, s0, 21
	s_add_i32 s0, 0, 0x25db0
	v_writelane_b32 v243, s0, 23
	s_add_i32 s0, s48, 0x820
	v_writelane_b32 v242, s0, 34
	s_add_i32 s0, s48, 0xc30
	v_writelane_b32 v242, s0, 35
	s_add_i32 s0, s48, 0x1040
	v_writelane_b32 v242, s0, 38
	s_add_i32 s0, s48, 0x1450
	v_writelane_b32 v242, s0, 24
	s_add_i32 s0, s48, 0x1860
	v_writelane_b32 v242, s0, 27
	v_add_u32_e32 v170, 0x6600, v164
	v_add_u32_e32 v171, 0x2a00, v165
	v_mov_b32_e32 v1, v128
	v_add_u32_e32 v105, 0x200, v104
	v_and_b32_e32 v174, -2, v8
	v_lshl_add_u64 v[130:131], s[44:45], 0, v[114:115]
	v_add_u32_e32 v115, 0xfffffe00, v104
	v_add_u32_e32 v176, s29, v172
	s_sub_i32 s42, 0, s33
	v_add_u32_e32 v177, 0x10900, v151
	v_sub_u32_e32 v178, 0, v119
	s_movk_i32 s55, 0x3000
	v_lshlrev_b32_e32 v132, 1, v112
	s_mov_b32 s44, 0x3f2aaaab
	v_mov_b32_e32 v179, 0x3ecc95a3
	s_mov_b32 s45, 0x3f317218
	s_mov_b32 s46, 0x7f800000
	s_mov_b32 s47, 0x33800000
	v_lshlrev_b32_e32 v134, 2, v118
	v_add_u32_e32 v181, v2, v114
	s_xor_b64 s[28:29], s[8:9], -1
	v_lshlrev_b32_e32 v110, 1, v4
	v_writelane_b32 v242, s48, 7
	s_add_i32 s0, s48, 0x1c70
	v_add_u32_e32 v182, v12, v14
	v_mov_b32_e32 v2, v111
	v_mov_b32_e32 v3, v111
	v_mov_b32_e32 v4, v111
	v_mov_b32_e32 v5, v111
	v_mov_b32_e32 v136, 0x3f317218
	v_mov_b32_e32 v183, 0x7f800000
	v_mov_b32_e32 v184, 0x7fc00000
	v_mov_b32_e32 v185, 0xff800000
	v_lshl_or_b32 v186, v180, 2, v7
	v_add_u32_e32 v187, v6, v14
	v_mov_b32_e32 v188, 0x7c
	v_writelane_b32 v242, s0, 29
	v_writelane_b32 v243, s53, 29
	s_branch .LBB0_3629

.LBB0_4989:
	s_or_b64 exec, exec, s[0:1]
	v_readlane_b32 s0, v243, 8
	v_readlane_b32 s1, v243, 9
	v_mov_b32_e32 v104, v0
	s_waitcnt lgkmcnt(0)
	v_mov_b32_e32 v1, s0
	v_mov_b32_e32 v2, s1
	s_barrier
	s_add_i32 s0, 0, 0x25d38
	v_readfirstlane_b32 s12, v2
	v_mov_b32_e32 v2, s79
	v_mov_b32_e32 v4, s77
	v_mov_b32_e32 v5, s78
	v_mov_b32_e32 v2, s0
	ds_read_b64 v[2:3], v2
	v_readfirstlane_b32 s50, v4
	v_readfirstlane_b32 s13, v1
	v_readfirstlane_b32 s44, v5
	s_mov_b32 s31, 0
	s_waitcnt lgkmcnt(0)
	v_readfirstlane_b32 s0, v2
	v_readfirstlane_b32 s1, v3
	s_cmpk_gt_i32 s50, 0xff
	v_writelane_b32 v243, s0, 27
	v_readfirstlane_b32 s8, v104
	s_nop 0
	v_writelane_b32 v243, s1, 28
	s_cbranch_scc1 .LBB0_5217
	v_readfirstlane_b32 s98, v0
	s_nop 3
	s_cmp_lt_u32 s98, 0x100
	s_cbranch_scc1 .Lp4prio3
	s_setprio 1
.Lp4prio3:
	s_add_u32 s0, s13, 0x7400000
	s_addc_u32 s1, s12, 0
	s_add_u32 s46, s13, 0x17e00000
	s_addc_u32 s47, s12, 0
	s_add_u32 s2, s13, 0x300000
	v_writelane_b32 v243, s80, 12
	v_writelane_b32 v242, s2, 45
	s_addc_u32 s2, s12, 0
	v_writelane_b32 v243, s81, 13
	v_writelane_b32 v242, s2, 47
	s_add_u32 s2, s13, 0x1a200000
	v_writelane_b32 v243, s2, 16
	s_addc_u32 s2, s12, 0
	s_ashr_i32 s26, s8, 6
	v_writelane_b32 v243, s2, 17
	s_mul_i32 s2, s26, 0x2080
	s_add_i32 s2, s2, 0
	s_add_i32 s48, s2, 0x14f00
	s_lshl_b32 s2, s50, 3
	s_add_i32 s45, s26, s2
	s_lshl_b32 s33, s44, 3
	s_cmpk_eq_i32 s44, 0x100
	s_cselect_b64 s[6:7], -1, 0
	s_and_b64 s[2:3], s[6:7], exec
	s_movk_i32 s3, 0x330
	v_cmp_gt_i32_e64 s[4:5], s3, v104
	v_and_b32_e32 v1, 3, v104
	s_cselect_b32 s16, 0x4800, 0
	v_writelane_b32 v242, s4, 13
	s_cselect_b32 s2, 3, 0
	s_lshl_b32 s17, s26, 4
	v_writelane_b32 v242, s5, 14
	v_cmp_eq_u32_e64 s[4:5], 0, v1
	v_ashrrev_i32_e32 v119, 2, v104
	s_movk_i32 s3, 0x70
	v_writelane_b32 v242, s4, 15
	s_cmp_gt_u32 s8, 63
	v_and_b32_e32 v107, 63, v104
	v_writelane_b32 v242, s5, 16
	s_movk_i32 s4, 0x8ff
	v_cmp_lt_i32_e64 s[4:5], s4, v104
	v_mul_lo_u32 v2, v119, s3
	v_add_u32_e32 v106, 0, v2
	v_writelane_b32 v242, s4, 17
	v_lshlrev_b32_e32 v2, 1, v107
	s_movk_i32 s14, 0xa0
	v_writelane_b32 v242, s5, 18
	s_cselect_b64 s[4:5], -1, 0
	s_cmp_lt_u32 s8, 64
	s_cselect_b64 s[8:9], -1, 0
	s_add_i32 s27, 0, 0x10700
	s_sub_i32 s18, 0, s16
	v_lshlrev_b32_e32 v108, 3, v1
	v_sub_u32_e32 v152, 0, v2
	v_mad_u64_u32 v[2:3], s[14:15], v119, s14, v[106:107]
	v_lshlrev_b32_e32 v114, 4, v1
	s_add_u32 s51, s13, 0x2ce00000
	v_and_b32_e32 v1, 7, v104
	v_bfe_u32 v154, v104, 3, 3
	s_addc_u32 s52, s12, 0
	v_mul_u32_u24_e32 v3, 0x410, v1
	v_lshlrev_b32_e32 v6, 2, v154
	s_add_i32 s12, 0, 0x8800
	v_add3_u32 v155, s48, v3, v6
	v_add_u32_e32 v3, s12, v108
	s_lshl_b32 s29, s26, 5
	s_mul_i32 s12, s44, 0x88
	s_add_i32 s29, s29, 0
	s_add_i32 s19, s45, s12
	s_cmp_lt_i32 s19, s16
	s_cselect_b64 s[42:43], -1, 0
	s_cmp_ge_i32 s19, s16
	s_cselect_b64 s[12:13], -1, 0
	s_and_b64 s[14:15], s[12:13], exec
	s_cselect_b32 s14, s18, s16
	v_bfe_u32 v109, v104, 4, 2
	s_add_i32 s18, s14, s19
	s_bfe_i32 s28, s2, 0x10000
	s_and_b32 s14, s2, 1
	v_and_b32_e32 v113, 15, v104
	v_writelane_b32 v242, s8, 41
	v_lshlrev_b32_e32 v118, 2, v109
	s_bitcmp1_b32 s2, 0
	v_or_b32_e32 v147, s17, v113
	v_writelane_b32 v242, s9, 42
	v_or_b32_e32 v8, s17, v118
	s_cselect_b64 s[16:17], -1, 0
	s_cmp_eq_u32 s14, 0
	v_writelane_b32 v242, s16, 31
	s_cselect_b64 s[14:15], -1, 0
	s_mul_hi_i32 s20, s18, 0x30c30c31
	v_writelane_b32 v242, s17, 32
	s_and_b64 s[16:17], s[14:15], exec
	s_mov_b32 s21, 0xc600000
	s_mov_b32 s16, 0xb800000
	s_cselect_b32 s30, s21, 0x8000000
	s_cselect_b32 s54, s16, 0x1000000
	s_or_b64 s[12:13], s[14:15], s[12:13]
	s_lshr_b32 s14, s20, 31
	s_ashr_i32 s34, s20, 10
	s_add_i32 s34, s34, s14
	s_mul_i32 s14, s34, 0xffffeb00
	s_add_i32 s41, s14, s18
	s_and_b64 s[14:15], s[12:13], exec
	s_cselect_b32 s35, s21, 0x8000000
	s_lshl_b32 s14, s41, 1
	s_add_i32 s14, s14, 0x7fffe400
	s_and_b32 s36, s14, 0x7fffffc0
	s_lshl_b32 s14, s19, 5
	s_and_b32 s37, s14, 0x3e0
	s_mul_hi_i32 s17, s41, 0x92492493
	s_and_b64 s[12:13], s[12:13], exec
	s_cselect_b32 s38, s16, 0x1000000
	s_add_i32 s17, s17, s41
	s_lshr_b32 s12, s17, 31
	s_ashr_i32 s13, s17, 7
	s_add_i32 s12, s13, s12
	s_mul_i32 s13, s12, 0xe0
	s_lshl_b32 s39, s12, 6
	s_sub_i32 s12, s41, s13
	s_lshl_b32 s40, s12, 5
	s_cmp_gt_i32 s26, -1
	s_cselect_b64 s[82:83], -1, 0
	s_cmp_gt_i32 s26, 0
	s_cselect_b64 s[12:13], -1, 0
	s_cmp_gt_i32 s26, 1
	s_cselect_b64 s[14:15], -1, 0
	s_cmp_gt_i32 s26, 2
	s_cselect_b64 s[16:17], -1, 0
	s_cmp_gt_i32 s26, 3
	s_cselect_b64 s[18:19], -1, 0
	s_cmp_gt_i32 s26, 4
	s_cselect_b64 s[20:21], -1, 0
	s_cmp_gt_i32 s26, 5
	s_cselect_b64 s[22:23], -1, 0
	s_cmp_gt_i32 s26, 6
	s_cselect_b64 s[24:25], -1, 0
	s_and_b64 s[42:43], s[6:7], s[42:43]
	v_writelane_b32 v242, s42, 43
	v_lshl_add_u32 v12, v8, 1, 0
	v_or_b32_e32 v8, 2, v118
	v_writelane_b32 v242, s43, 44
	v_cmp_gt_i32_e64 s[42:43], v118, v147
	v_bfe_u32 v5, v104, 2, 2
	v_lshlrev_b32_e32 v112, 3, v109
	v_writelane_b32 v243, s42, 31
	v_lshlrev_b32_e32 v7, 2, v107
	v_add_u32_e32 v149, s27, v7
	v_writelane_b32 v243, s43, 32
	v_cmp_lt_i32_e64 s[42:43], v118, v147
	v_add_u32_e32 v151, 0, v7
	v_and_b32_e32 v159, 28, v7
	v_writelane_b32 v243, s42, 33
	v_or_b32_e32 v7, v112, v5
	v_or_b32_e32 v5, v118, v5
	v_writelane_b32 v243, s43, 34
	v_cmp_gt_i32_e64 s[42:43], v8, v147
	v_or_b32_e32 v8, 3, v118
	s_cmpk_lt_i32 s41, 0xe00
	v_writelane_b32 v243, s42, 35
	v_mad_u32_u24 v160, v5, s3, v3
	v_mul_u32_u24_e32 v5, 0x110, v7
	v_writelane_b32 v243, s43, 36
	v_cmp_gt_i32_e64 s[42:43], v8, v147
	v_or_b32_e32 v8, 16, v118
	v_add3_u32 v164, s29, v108, v5
	v_writelane_b32 v243, s42, 37
	s_cselect_b32 s29, s40, s37
	s_mov_b32 s37, 0xe00000
	v_writelane_b32 v243, s43, 38
	v_cmp_gt_i32_e64 s[42:43], v8, v147
	v_or_b32_e32 v8, 17, v118
	v_mad_u32_u24 v165, v7, s3, v3
	v_writelane_b32 v243, s42, 39
	s_movk_i32 s3, 0x400
	s_cselect_b32 s35, s38, s35
	v_writelane_b32 v243, s43, 40
	v_cmp_gt_i32_e64 s[42:43], v8, v147
	v_or_b32_e32 v8, 18, v118
	s_cselect_b32 s37, s37, 0x700000
	v_writelane_b32 v243, s42, 41
	s_cselect_b32 s3, s3, 0xe00
	s_cselect_b32 s36, s39, s36
	v_writelane_b32 v243, s43, 42
	v_cmp_gt_i32_e64 s[42:43], v8, v147
	v_or_b32_e32 v8, 19, v118
	s_mul_hi_i32 s38, s37, s34
	v_writelane_b32 v243, s42, 43
	s_mul_i32 s37, s37, s34
	s_add_u32 s34, s51, s35
	v_writelane_b32 v243, s43, 44
	v_cmp_gt_i32_e64 s[42:43], v8, v147
	v_or_b32_e32 v8, 32, v118
	s_addc_u32 s35, s52, 0
	v_writelane_b32 v243, s42, 45
	s_add_u32 s39, s34, s37
	s_addc_u32 s38, s35, s38
	v_writelane_b32 v243, s43, 46
	v_cmp_gt_i32_e64 s[42:43], v8, v147
	v_or_b32_e32 v8, 33, v118
	s_ashr_i32 s37, s36, 31
	v_writelane_b32 v243, s42, 47
	s_lshl_b64 s[34:35], s[36:37], 1
	v_mov_b32_e32 v111, 0
	v_writelane_b32 v243, s43, 48
	v_cmp_gt_i32_e64 s[42:43], v8, v147
	v_or_b32_e32 v8, 34, v118
	v_and_b32_e32 v110, 48, v104
	v_writelane_b32 v243, s42, 49
	s_add_u32 s34, s39, s34
	v_lshlrev_b32_e32 v4, 3, v1
	v_writelane_b32 v243, s43, 50
	v_cmp_gt_i32_e64 s[42:43], v8, v147
	v_or_b32_e32 v8, 35, v118
	v_or_b32_e32 v156, 8, v154
	v_writelane_b32 v243, s42, 51
	v_lshl_add_u64 v[116:117], s[46:47], 0, v[110:111]
	v_add_u32_e32 v6, 0, v110
	v_writelane_b32 v243, s43, 52
	v_cmp_gt_i32_e64 s[42:43], v8, v147
	v_or_b32_e32 v8, 48, v118
	s_addc_u32 s35, s38, s35
	v_writelane_b32 v243, s42, 53
	v_lshlrev_b32_e32 v110, 4, v1
	v_or_b32_e32 v1, s29, v154
	v_writelane_b32 v243, s43, 54
	v_cmp_gt_i32_e64 s[42:43], v8, v147
	v_or_b32_e32 v8, 49, v118
	v_or_b32_e32 v157, 16, v154
	v_writelane_b32 v243, s42, 55
	v_or_b32_e32 v158, 24, v154
	s_lshr_b32 s2, s2, 1
	v_writelane_b32 v243, s43, 56
	v_cmp_gt_i32_e64 s[42:43], v8, v147
	v_or_b32_e32 v8, 50, v118
	v_lshlrev_b32_e32 v172, 2, v104
	v_writelane_b32 v243, s42, 57
	v_add_u32_e32 v3, 0, v172
	v_add_u32_e32 v3, 0x12b00, v3
	v_writelane_b32 v243, s43, 58
	v_cmp_gt_i32_e64 s[42:43], v8, v147
	v_or_b32_e32 v8, 51, v118
	s_lshl_b32 s41, s44, 4
	v_writelane_b32 v243, s42, 59
	v_and_b32_e32 v13, 0x7f, v104
	v_mul_u32_u24_e32 v14, 0x110, v113
	v_writelane_b32 v243, s43, 60
	v_cmp_gt_i32_e64 s[42:43], v8, v147
	v_or_b32_e32 v8, 64, v118
	v_or_b32_e32 v128, 0xffffff00, v13
	v_writelane_b32 v243, s42, 61
	v_mov_b32_e32 v115, v111
	v_mbcnt_hi_u32_b32 v180, -1, v212
	v_writelane_b32 v243, s43, 62
	v_cmp_gt_i32_e64 s[42:43], v8, v147
	v_or_b32_e32 v8, 0x41, v118
	s_movk_i32 s49, 0x100
	v_writelane_b32 v243, s42, 63
	v_writelane_b32 v243, s30, 14
	s_mov_b32 s55, s31
	v_writelane_b32 v242, s43, 0
	v_cmp_gt_i32_e64 s[42:43], v8, v147
	v_or_b32_e32 v8, 0x42, v118
	v_writelane_b32 v243, s31, 15
	v_writelane_b32 v242, s42, 1
	v_writelane_b32 v243, s44, 29
	v_sub_u32_e32 v129, 0xff, v119
	v_writelane_b32 v242, s43, 2
	v_cmp_gt_i32_e64 s[42:43], v8, v147
	v_or_b32_e32 v8, 0x43, v118
	v_sub_u32_e32 v148, 0xff, v147
	v_writelane_b32 v242, s42, 3
	v_add_u32_e32 v150, 0x100, v149
	v_cmp_lt_u32_e64 s[8:9], 15, v107
	v_writelane_b32 v242, s43, 4
	v_cmp_gt_i32_e64 s[42:43], v8, v147
	v_or_b32_e32 v8, 0x50, v118
	v_cmp_eq_u32_e64 s[10:11], 0, v107
	v_writelane_b32 v242, s42, 5
	v_add_u32_e32 v153, 0xffffff00, v147
	v_add_u32_e32 v161, 0xe00, v160
	v_writelane_b32 v242, s43, 6
	v_cmp_gt_i32_e64 s[42:43], v8, v147
	v_or_b32_e32 v8, 0x51, v118
	v_cmp_gt_i32_e64 s[56:57], v8, v147
	v_or_b32_e32 v8, 0x52, v118
	v_cmp_gt_i32_e64 s[58:59], v8, v147
	v_or_b32_e32 v8, 0x53, v118
	v_cmp_gt_i32_e64 s[60:61], v8, v147
	v_or_b32_e32 v8, 0x60, v118
	v_cmp_gt_i32_e64 s[62:63], v8, v147
	v_or_b32_e32 v8, 0x61, v118
	v_cmp_gt_i32_e64 s[64:65], v8, v147
	v_or_b32_e32 v8, 0x62, v118
	v_cmp_gt_i32_e64 s[66:67], v8, v147
	v_or_b32_e32 v8, 0x63, v118
	v_cmp_gt_i32_e64 s[68:69], v8, v147
	v_or_b32_e32 v8, 0x70, v118
	v_cmp_gt_i32_e64 s[70:71], v8, v147
	v_or_b32_e32 v8, 0x71, v118
	v_cmp_gt_i32_e64 s[72:73], v8, v147
	v_or_b32_e32 v8, 0x72, v118
	v_cmp_gt_i32_e64 s[74:75], v8, v147
	v_or_b32_e32 v8, 0x73, v118
	v_writelane_b32 v242, s42, 11
	v_cmp_gt_i32_e64 s[76:77], v8, v147
	v_lshl_add_u64 v[8:9], s[34:35], 0, v[110:111]
	v_mad_i64_i32 v[10:11], s[34:35], s3, v1, 0
	v_or_b32_e32 v1, s29, v156
	v_writelane_b32 v242, s43, 12
	v_lshl_add_u64 v[120:121], v[10:11], 1, v[8:9]
	v_mad_i64_i32 v[10:11], s[34:35], s3, v1, 0
	v_or_b32_e32 v1, s29, v157
	v_writelane_b32 v242, s51, 9
	v_lshl_add_u64 v[122:123], v[10:11], 1, v[8:9]
	v_mad_i64_i32 v[10:11], s[34:35], s3, v1, 0
	v_or_b32_e32 v1, s29, v158
	v_writelane_b32 v242, s52, 30
	v_lshl_add_u64 v[124:125], v[10:11], 1, v[8:9]
	v_mad_i64_i32 v[10:11], s[34:35], s3, v1, 0
	s_lshl_b32 s3, s45, 5
	v_max_i32_e32 v1, 0x700, v104
	v_writelane_b32 v242, s45, 19
	s_and_b32 s3, s3, 0x3e0
	v_sub_u32_e32 v1, v1, v104
	v_writelane_b32 v242, s3, 36
	v_add_u32_e32 v1, 0x1ff, v1
	v_writelane_b32 v242, s54, 39
	s_and_b32 s3, s28, 3
	v_lshrrev_b32_e32 v5, 9, v1
	v_writelane_b32 v242, s55, 40
	s_lshl_b32 s2, s2, s3
	v_add_u32_e32 v7, 1, v5
	v_add_u32_e32 v5, -1, v5
	v_lshl_add_u64 v[126:127], v[10:11], 1, v[8:9]
	v_writelane_b32 v242, s2, 33
	v_lshlrev_b32_e32 v9, 2, v1
	v_cmp_lt_u32_e64 s[28:29], 1, v5
	v_lshrrev_b32_e32 v8, 1, v5
	s_movk_i32 s2, 0xdff
	v_and_b32_e32 v9, 0xfffff800, v9
	v_writelane_b32 v242, s28, 53
	v_and_b32_e32 v5, 2, v5
	v_cmp_lt_u32_e32 vcc, s2, v1
	v_cmp_gt_u32_e64 s[2:3], 2.0, v1
	v_add_u32_e32 v1, v3, v9
	v_writelane_b32 v242, s29, 54
	v_cmp_eq_u32_e64 s[28:29], 0, v5
	v_cmp_ge_u32_e64 s[78:79], v1, v3
	v_and_b32_e32 v3, 0xfffffe, v7
	v_writelane_b32 v242, s28, 55
	s_and_b64 s[2:3], s[78:79], s[2:3]
	s_and_b64 s[2:3], vcc, s[2:3]
	v_writelane_b32 v242, s29, 56
	v_cmp_ne_u32_e64 s[28:29], v7, v3
	v_lshl_add_u32 v173, v3, 9, v104
	v_lshl_add_u32 v3, v104, 4, 0
	v_writelane_b32 v242, s28, 57
	v_add_u32_e32 v8, 1, v8
	v_add_u32_e32 v175, 0xc000, v3
	v_writelane_b32 v242, s29, 58
	v_writelane_b32 v242, s2, 49
	v_bfrev_b32_e32 v7, 0.5
	v_add_u32_e32 v162, 0x1c00, v160
	v_writelane_b32 v242, s3, 50
	v_writelane_b32 v242, s46, 25
	s_sub_i32 s2, 0, s41
	s_lshl_b32 s3, s26, 1
	v_writelane_b32 v242, s47, 26
	v_writelane_b32 v242, s2, 23
	s_lshl_b32 s2, s50, 4
	s_add_i32 s2, s2, s3
	s_add_i32 s2, s2, 0x80007400
	v_writelane_b32 v242, s2, 51
	s_add_i32 s2, 0, 0x25de0
	v_writelane_b32 v242, s2, 21
	s_add_i32 s2, 0, 0x25db8
	v_writelane_b32 v243, s2, 19
	s_add_i32 s2, 0, 0x25dd0
	v_writelane_b32 v243, s2, 20
	s_add_i32 s2, 0, 0x25da8
	v_writelane_b32 v242, s2, 10
	s_add_i32 s2, 0, 0x25dd8
	v_writelane_b32 v243, s2, 21
	s_add_i32 s2, 0, 0x25db0
	v_writelane_b32 v243, s2, 23
	s_add_i32 s2, s48, 0x820
	v_writelane_b32 v242, s2, 34
	s_add_i32 s2, s48, 0xc30
	v_writelane_b32 v242, s2, 35
	s_add_i32 s2, s48, 0x1040
	v_writelane_b32 v242, s2, 38
	s_add_i32 s2, s48, 0x1450
	v_writelane_b32 v242, s2, 24
	s_add_i32 s2, s48, 0x1860
	v_writelane_b32 v242, s2, 27
	v_add_u32_e32 v163, 0x2a00, v160
	v_add_u32_e32 v166, 0x2200, v164
	v_add_u32_e32 v167, 0xe00, v165
	v_add_u32_e32 v168, 0x4400, v164
	v_add_u32_e32 v169, 0x1c00, v165
	v_add_u32_e32 v170, 0x6600, v164
	v_add_u32_e32 v171, 0x2a00, v165
	v_mov_b32_e32 v1, v128
	v_add_u32_e32 v105, 0x200, v104
	v_and_b32_e32 v174, -2, v8
	v_lshl_add_u64 v[130:131], s[46:47], 0, v[114:115]
	v_add_u32_e32 v115, 0xfffffe00, v104
	v_add_u32_e32 v176, s27, v172
	s_sub_i32 s40, 0, s33
	v_add_u32_e32 v177, 0x10900, v151
	v_sub_u32_e32 v178, 0, v119
	v_lshlrev_b32_e32 v132, 1, v112
	s_mov_b32 s42, 0x3f2aaaab
	v_mov_b32_e32 v179, 0x3ecc95a3
	s_mov_b32 s43, 0x3f317218
	s_mov_b32 s44, 0x7f800000
	s_mov_b32 s45, 0x33800000
	v_lshlrev_b32_e32 v134, 2, v118
	v_add_u32_e32 v181, v2, v114
	s_xor_b64 s[26:27], s[6:7], -1
	v_lshlrev_b32_e32 v110, 1, v4
	v_writelane_b32 v242, s48, 7
	s_add_i32 s2, s48, 0x1c70
	v_add_u32_e32 v182, v12, v14
	v_mov_b32_e32 v2, v111
	v_mov_b32_e32 v3, v111
	v_mov_b32_e32 v4, v111
	v_mov_b32_e32 v5, v111
	v_mov_b32_e32 v136, 0x3f317218
	v_mov_b32_e32 v183, 0x7f800000
	v_mov_b32_e32 v184, 0x7fc00000
	v_mov_b32_e32 v185, 0xff800000
	v_lshl_or_b32 v186, v180, 2, v7
	v_add_u32_e32 v187, v6, v14
	v_mov_b32_e32 v188, 0x7c
	v_writelane_b32 v242, s2, 29
	s_branch .LBB0_4992
